# side-workgroup conversion loop: done-flag load and queue atomic in flight together (one round trip less per entry)
# speedup vs baseline: 1.0069x; 1.0058x over previous
;     ...
;     for (;;) {
;         if (tid == 0) bc[par] = nxt;
;         __syncthreads();
;         const unsigned cur = __builtin_amdgcn_readfirstlane(bc[par]); par ^= 2;
;         if (cur == CQ_END) break;
.LBB0_136:
	s_and_saveexec_b64 s[6:7], s[0:1]
	s_lshl_b32 s8, s19, 2
	s_add_i32 s8, s8, 0
	s_add_i32 s8, s8, 0x20040
	v_mov_b32_e32 v2, s8
	ds_write_b32 v2, v129
	s_or_b64 exec, exec, s[6:7]
	s_lshl_b32 s6, s19, 2
	s_add_i32 s6, s6, 0
	s_add_i32 s6, s6, 0x20040
	v_mov_b32_e32 v2, s6
	s_waitcnt lgkmcnt(0)
	s_barrier
	ds_read_b32 v2, v2
	v_readfirstlane_b32 s8, v0
	s_waitcnt lgkmcnt(0)
	v_readfirstlane_b32 s20, v2
	s_cmp_eq_u32 s20, -1
	s_cbranch_scc1 .LBB0_155
	s_and_saveexec_b64 s[6:7], s[0:1]
	s_cbranch_execz .LBB0_151
	v_cmp_lt_i32_e32 vcc, 1, v1
	s_and_saveexec_b64 s[8:9], vcc
	s_cbranch_execz .LBB0_142
	global_load_dword v6, v187, s[4:5] sc1

; __device__ __forceinline__ unsigned xb_add(unsigned* p, unsigned v) { return __hip_atomic_fetch_add(p, v, __ATOMIC_RELAXED, __HIP_MEMORY_SCOPE_AGENT); }
; __device__ __forceinline__ unsigned convq_take(unsigned* ctl, bool allow2) {
;     unsigned it = xb_add(ctl + CW_Q, 1u); if (it < (unsigned)CQ_M13) return it;
;     if (allow2) { it = xb_add(ctl + CW_Q + 32, 1u); if (it < (unsigned)CQ_M2) return 0x80000000u | it; }
;     return CQ_END;
; }
.LBB0_145:
	s_or_b64 exec, exec, s[10:11]
	s_waitcnt vmcnt(0)
	v_cmp_gt_u32_e32 vcc, 16, v6
	s_nop 1
	v_cndmask_b32_e32 v1, 1, v1, vcc
	v_readfirstlane_b32 s10, v3
	s_nop 1
	v_add_u32_e32 v129, s10, v2
	s_movk_i32 s10, 0xdff
	v_cmp_lt_u32_e32 vcc, s10, v129
	s_and_saveexec_b64 s[10:11], vcc
	s_cbranch_execz .LBB0_149
	s_mov_b64 s[16:17], exec
	v_mbcnt_lo_u32_b32 v2, s16, 0
	v_mbcnt_hi_u32_b32 v2, s17, v2
	v_cmp_eq_u32_e32 vcc, 0, v2
	s_and_saveexec_b64 s[12:13], vcc
	s_cbranch_execz .LBB0_148
	s_bcnt1_i32_b64 s14, s[16:17]
	v_mov_b32_e32 v3, s14
	v_readlane_b32 s14, v250, 20
	v_readlane_b32 s15, v250, 21
	s_nop 4
	global_atomic_add v3, v187, v3, s[14:15] sc0

;     ...
;     for (;;) {
;         if (tid == 0) bc[par] = nxt;
;         __syncthreads();
;         const unsigned cur = __builtin_amdgcn_readfirstlane(bc[par]); par ^= 2;
;         if (cur == CQ_END) break;
.LBB0_1066:
	s_and_saveexec_b64 s[4:5], s[0:1]
	s_lshl_b32 s6, s17, 2
	s_add_i32 s6, s6, 0
	s_add_i32 s6, s6, 0x20040
	v_mov_b32_e32 v2, s6
	ds_write_b32 v2, v129
	s_or_b64 exec, exec, s[4:5]
	s_lshl_b32 s4, s17, 2
	s_add_i32 s4, s4, 0
	s_add_i32 s4, s4, 0x20040
	v_mov_b32_e32 v2, s4
	s_waitcnt lgkmcnt(0)
	s_barrier
	ds_read_b32 v2, v2
	v_readfirstlane_b32 s6, v0
	s_waitcnt lgkmcnt(0)
	v_readfirstlane_b32 s18, v2
	s_cmp_eq_u32 s18, -1
	s_cbranch_scc1 .LBB0_1085
	s_and_saveexec_b64 s[4:5], s[0:1]
	s_cbranch_execz .LBB0_1081
	v_cmp_lt_i32_e32 vcc, 1, v127
	s_and_saveexec_b64 s[6:7], vcc
	s_cbranch_execz .LBB0_1072
	v_readlane_b32 s8, v252, 35
	v_readlane_b32 s9, v252, 36
	s_nop 4
	global_load_dword v6, v187, s[8:9] sc1

; __device__ __forceinline__ unsigned xb_add(unsigned* p, unsigned v) { return __hip_atomic_fetch_add(p, v, __ATOMIC_RELAXED, __HIP_MEMORY_SCOPE_AGENT); }
; __device__ __forceinline__ unsigned convq_take(unsigned* ctl, bool allow2) {
;     unsigned it = xb_add(ctl + CW_Q, 1u); if (it < (unsigned)CQ_M13) return it;
;     if (allow2) { it = xb_add(ctl + CW_Q + 32, 1u); if (it < (unsigned)CQ_M2) return 0x80000000u | it; }
;     return CQ_END;
; }
.LBB0_1075:
	s_or_b64 exec, exec, s[8:9]
	s_waitcnt vmcnt(0)
	v_cmp_gt_u32_e32 vcc, 16, v6
	s_nop 1
	v_cndmask_b32_e32 v127, 1, v127, vcc
	v_readfirstlane_b32 s8, v3
	s_nop 1
	v_add_u32_e32 v129, s8, v2
	s_movk_i32 s8, 0xdff
	v_cmp_lt_u32_e32 vcc, s8, v129
	s_and_saveexec_b64 s[8:9], vcc
	s_cbranch_execz .LBB0_1079
	s_mov_b64 s[12:13], exec
	v_mbcnt_lo_u32_b32 v2, s12, 0
	v_mbcnt_hi_u32_b32 v2, s13, v2
	v_cmp_eq_u32_e32 vcc, 0, v2
	s_and_saveexec_b64 s[10:11], vcc
	s_cbranch_execz .LBB0_1078
	s_bcnt1_i32_b64 s12, s[12:13]
	v_mov_b32_e32 v3, s12
	v_readlane_b32 s12, v250, 20
	v_readlane_b32 s13, v250, 21
	s_nop 4
	global_atomic_add v3, v187, v3, s[12:13] sc0

;     ...
;     for (;;) {
;         if (tid == 0) bc[par] = nxt;
;         __syncthreads();
;         const unsigned cur = __builtin_amdgcn_readfirstlane(bc[par]); par ^= 2;
;         if (cur == CQ_END) break;
.LBB0_1152:
	s_and_saveexec_b64 s[4:5], s[0:1]
	s_lshl_b32 s6, s17, 2
	s_add_i32 s6, s6, 0
	s_add_i32 s6, s6, 0x20040
	v_mov_b32_e32 v2, s6
	ds_write_b32 v2, v129
	s_or_b64 exec, exec, s[4:5]
	s_lshl_b32 s4, s17, 2
	s_add_i32 s4, s4, 0
	s_add_i32 s4, s4, 0x20040
	v_mov_b32_e32 v2, s4
	s_waitcnt vmcnt(0) lgkmcnt(0)
	s_barrier
	ds_read_b32 v2, v2
	v_readfirstlane_b32 s6, v0
	s_waitcnt lgkmcnt(0)
	v_readfirstlane_b32 s18, v2
	s_cmp_eq_u32 s18, -1
	s_cbranch_scc1 .LBB0_1171
	s_and_saveexec_b64 s[4:5], s[0:1]
	s_cbranch_execz .LBB0_1167
	v_cmp_lt_i32_e32 vcc, 1, v127
	s_and_saveexec_b64 s[6:7], vcc
	s_cbranch_execz .LBB0_1158
	v_readlane_b32 s8, v252, 41
	v_readlane_b32 s9, v252, 42
	s_nop 4
	global_load_dword v6, v187, s[8:9] sc1
